# NSA: window-loop loads hoisted above waits, phase-C read-modify-write batched, phase-B TURN waits polled in parallel
# speedup vs baseline: 1.1326x; 1.1326x over previous
.LBB0_637:
	s_sub_i32 s65, s64, 64
	s_sub_i32 s66, s64, 32
	s_cmp_lt_i32 s65, s15
	s_cselect_b64 s[16:17], -1, 0
	s_and_b64 s[18:19], s[16:17], exec
	s_cselect_b32 s18, s66, s65
	s_add_i32 s18, s18, s14
	s_ashr_i32 s19, s18, 31
	s_lshl_b64 s[18:19], s[18:19], 7
	v_lshl_add_u64 v[58:59], v[148:149], 0, s[18:19]
	v_lshl_add_u64 v[66:67], v[146:147], 0, s[18:19]
	global_load_dwordx4 v[110:113], v[58:59], off
	global_load_dwordx4 v[106:109], v[58:59], off offset:1024
	global_load_dwordx4 v[102:105], v[58:59], off offset:2048
	global_load_dwordx4 v[98:101], v[58:59], off offset:3072
	global_load_dwordx4 v[54:57], v[66:67], off
	global_load_dwordx4 v[58:61], v[66:67], off offset:1024
	global_load_dwordx4 v[62:65], v[66:67], off offset:2048
	s_nop 0
	global_load_dwordx4 v[66:69], v[66:67], off offset:3072
	s_waitcnt vmcnt(8)
	v_mfma_f32_16x16x32_bf16 v[216:219], v[78:81], v[10:13], 0
	v_mfma_f32_16x16x32_bf16 v[74:77], v[74:77], v[14:17], v[216:219]
	v_add_u32_e32 v78, s36, v198
	v_mfma_f32_16x16x32_bf16 v[70:73], v[70:73], v[10:13], 0
	v_add_u32_e32 v80, 0x1fbb4, v78
	s_add_i32 s66, s14, s64
	s_sub_i32 s18, s66, 64
	v_mfma_f32_16x16x32_bf16 v[50:53], v[50:53], v[14:17], v[70:73]
	s_cmp_gt_i32 s18, s63
	s_cselect_b64 s[18:19], -1, 0
	s_cmpk_gt_i32 s9, 0x1fc
	s_nop 0
	v_add_u32_e32 v70, 0x1fbfc, v78
	v_add_u32_e32 v72, 0x1fbbc, v78
	v_add_u32_e32 v78, 0x1fbf4, v78
	ds_read2_b32 v[70:71], v70 offset1:1
	ds_read2_b32 v[72:73], v72 offset1:1
	ds_read2_b32 v[78:79], v78 offset1:1
	ds_read2_b32 v[80:81], v80 offset1:1
	s_cselect_b64 s[68:69], -1, 0
	s_or_b64 s[68:69], s[18:19], s[68:69]
	s_waitcnt lgkmcnt(3)
	v_add_f32_e32 v90, v74, v71
	s_waitcnt lgkmcnt(2)
	v_add_f32_e32 v86, v50, v73
	v_add_f32_e32 v89, v75, v70
	v_add_f32_e32 v85, v51, v72
	s_waitcnt lgkmcnt(1)
	v_add_f32_e32 v88, v76, v79
	s_waitcnt lgkmcnt(0)
	v_add_f32_e32 v82, v52, v81
	v_add_f32_e32 v87, v77, v78
	v_add_f32_e32 v81, v53, v80
	v_exp_f32_e32 v51, v90
	v_exp_f32_e32 v52, v89
	v_exp_f32_e32 v53, v88
	v_exp_f32_e32 v70, v87
	v_exp_f32_e32 v71, v86
	v_exp_f32_e32 v72, v85
	v_exp_f32_e32 v73, v82
	v_exp_f32_e32 v74, v81
	v_add_u32_e32 v214, s9, v192
	s_mov_b64 s[18:19], -1
	s_and_b64 vcc, exec, s[68:69]
	s_cbranch_vccz .LBB0_639
	v_exp_f32_e32 v75, v90
	v_exp_f32_e32 v79, v89
	v_add_u32_e32 v76, -1, v214
	v_cmp_gt_u32_e32 vcc, s88, v214
	v_exp_f32_e32 v87, v87
	v_add_u32_e32 v77, -2, v214
	v_cndmask_b32_e32 v75, 0, v75, vcc
	v_cmp_gt_u32_e32 vcc, s88, v76
	v_exp_f32_e32 v86, v86
	v_add_u32_e32 v78, -3, v214
	v_cndmask_b32_e32 v76, 0, v79, vcc
	v_exp_f32_e32 v79, v88
	v_add_f32_e32 v89, 0, v75
	v_cmp_gt_u32_e32 vcc, s88, v77
	v_exp_f32_e32 v85, v85
	v_add_u32_e32 v50, -16, v214
	v_add_f32_e32 v88, v89, v76
	v_cndmask_b32_e32 v77, 0, v79, vcc
	v_cmp_gt_u32_e32 vcc, s88, v78
	v_exp_f32_e32 v82, v82
	v_subrev_u32_e32 v80, 17, v214
	v_add_f32_e32 v79, v88, v77
	v_cndmask_b32_e32 v78, 0, v87, vcc
	v_cmp_gt_u32_e32 vcc, s88, v50
	v_exp_f32_e32 v81, v81
	v_subrev_u32_e32 v83, 18, v214
	v_add_f32_e32 v87, v79, v78
	v_cndmask_b32_e32 v79, 0, v86, vcc
	v_cmp_gt_u32_e32 vcc, s88, v80
	v_subrev_u32_e32 v84, 19, v214
	v_add_f32_e32 v50, v79, v87
	v_cndmask_b32_e32 v80, 0, v85, vcc
	v_cmp_gt_u32_e32 vcc, s88, v83
	v_add_f32_e32 v50, v80, v50
	s_mov_b64 s[18:19], 0
	v_cndmask_b32_e32 v83, 0, v82, vcc
	v_cmp_gt_u32_e32 vcc, s88, v84
	v_add_f32_e32 v50, v83, v50
	s_nop 0
	v_cndmask_b32_e32 v84, 0, v81, vcc
	v_add_f32_e32 v50, v84, v50

.LBB0_641:
	v_add_u32_e32 v215, v174, v177
	ds_write_b128 v215, v[30:33]
	ds_write_b128 v215, v[26:29] offset:1152
	ds_write_b128 v215, v[22:25] offset:2304
	ds_write_b128 v215, v[18:21] offset:3456
	v_cvt_pk_bf16_f32 v18, v75, v76
	v_cvt_pk_bf16_f32 v19, v77, v78
	v_cvt_pk_bf16_f32 v20, v79, v80
	v_cvt_pk_bf16_f32 v21, v83, v84
	ds_read_b64_tr_b16 v[24:25], v207
	ds_read_b64_tr_b16 v[22:23], v206
	ds_read_b64_tr_b16 v[26:27], v206 offset:32
	ds_read_b64_tr_b16 v[30:31], v206 offset:64
	ds_read_b64_tr_b16 v[70:71], v206 offset:96
	ds_read_b64_tr_b16 v[28:29], v207 offset:32
	ds_read_b64_tr_b16 v[32:33], v207 offset:64
	ds_read_b64_tr_b16 v[72:73], v207 offset:96
	s_waitcnt lgkmcnt(6)
	v_mfma_f32_16x16x32_bf16 v[82:85], v[18:21], v[22:25], v[46:49]
	v_add_f32_e32 v213, v212, v50
	s_mov_b64 s[18:19], -1
	s_waitcnt lgkmcnt(2)
	v_mfma_f32_16x16x32_bf16 v[86:89], v[18:21], v[26:29], v[42:45]
	s_andn2_b64 vcc, exec, s[16:17]
	s_mov_b64 s[16:17], -1
	s_waitcnt lgkmcnt(1)
	v_mfma_f32_16x16x32_bf16 v[94:97], v[18:21], v[30:33], v[38:41]
	s_waitcnt lgkmcnt(0)
	v_mfma_f32_16x16x32_bf16 v[90:93], v[18:21], v[70:73], v[34:37]
	s_cbranch_vccnz .LBB0_636
	s_cmp_gt_i32 s64, s15
	s_cselect_b64 s[16:17], -1, 0
	s_and_b64 s[18:19], s[16:17], exec
	s_cselect_b32 s18, s65, s64
	s_add_i32 s18, s18, s14
	s_ashr_i32 s19, s18, 31
	s_lshl_b64 s[18:19], s[18:19], 7
	v_lshl_add_u64 v[22:23], v[148:149], 0, s[18:19]
	v_lshl_add_u64 v[18:19], v[146:147], 0, s[18:19]
	global_load_dwordx4 v[78:81], v[22:23], off
	global_load_dwordx4 v[74:77], v[22:23], off offset:1024
	global_load_dwordx4 v[70:73], v[22:23], off offset:2048
	global_load_dwordx4 v[50:53], v[22:23], off offset:3072
	global_load_dwordx4 v[30:33], v[18:19], off
	global_load_dwordx4 v[26:29], v[18:19], off offset:1024
	global_load_dwordx4 v[22:25], v[18:19], off offset:2048
	s_nop 0
	global_load_dwordx4 v[18:21], v[18:19], off offset:3072
	s_waitcnt vmcnt(15)
	v_mfma_f32_16x16x32_bf16 v[220:223], v[110:113], v[10:13], 0
	s_waitcnt vmcnt(14)
	v_mfma_f32_16x16x32_bf16 v[34:37], v[106:109], v[14:17], v[220:223]
	v_add_u32_e32 v46, s36, v211
	v_add_u32_e32 v48, 0x1fb34, v46
	v_add_u32_e32 v42, 0x1fb7c, v46
	s_waitcnt vmcnt(13)
	v_mfma_f32_16x16x32_bf16 v[38:41], v[102:105], v[10:13], 0
	v_add_u32_e32 v44, 0x1fb3c, v46
	v_add_u32_e32 v46, 0x1fb74, v46
	ds_read2_b32 v[42:43], v42 offset1:1
	ds_read2_b32 v[44:45], v44 offset1:1
	ds_read2_b32 v[46:47], v46 offset1:1
	ds_read2_b32 v[48:49], v48 offset1:1
	s_waitcnt vmcnt(12)
	v_mfma_f32_16x16x32_bf16 v[38:41], v[98:101], v[14:17], v[38:41]
	s_sub_i32 s18, s66, 32
	s_cmp_gt_i32 s18, s63
	s_waitcnt lgkmcnt(3)
	v_add_f32_e32 v106, v34, v43
	v_add_f32_e32 v105, v35, v42
	s_waitcnt lgkmcnt(1)
	v_add_f32_e32 v104, v36, v47
	s_nop 0
	v_add_f32_e32 v102, v38, v45
	v_add_f32_e32 v101, v39, v44
	s_waitcnt lgkmcnt(0)
	v_add_f32_e32 v99, v40, v49
	v_add_f32_e32 v103, v37, v46
	v_add_f32_e32 v48, v41, v48
	s_cselect_b64 s[18:19], -1, 0
	s_sub_i32 s65, s9, 32
	s_cmpk_gt_i32 s65, 0x1fc
	v_exp_f32_e32 v34, v106
	v_exp_f32_e32 v35, v105
	v_exp_f32_e32 v36, v104
	v_exp_f32_e32 v37, v103
	v_exp_f32_e32 v38, v102
	v_exp_f32_e32 v39, v101
	v_exp_f32_e32 v40, v99
	v_exp_f32_e32 v41, v48
	s_cselect_b64 s[66:67], -1, 0
	s_or_b64 s[66:67], s[18:19], s[66:67]
	s_mov_b64 s[18:19], -1
	s_and_b64 vcc, exec, s[66:67]
	s_cbranch_vccz .LBB0_644
	v_exp_f32_e32 v98, v106
	v_exp_f32_e32 v105, v105
	v_subrev_u32_e32 v42, 32, v214
	v_exp_f32_e32 v104, v104
	v_subrev_u32_e32 v43, 33, v214
	v_cmp_gt_u32_e32 vcc, s88, v42
	v_exp_f32_e32 v103, v103
	v_subrev_u32_e32 v44, 34, v214
	v_cndmask_b32_e32 v42, 0, v98, vcc
	v_cmp_gt_u32_e32 vcc, s88, v43
	v_exp_f32_e32 v102, v102
	v_subrev_u32_e32 v45, 35, v214
	v_add_f32_e32 v98, 0, v42
	v_cndmask_b32_e32 v43, 0, v105, vcc
	v_cmp_gt_u32_e32 vcc, s88, v44
	v_exp_f32_e32 v101, v101
	v_subrev_u32_e32 v46, 48, v214
	v_add_f32_e32 v98, v98, v43
	v_cndmask_b32_e32 v44, 0, v104, vcc
	v_cmp_gt_u32_e32 vcc, s88, v45
	v_exp_f32_e32 v99, v99
	v_subrev_u32_e32 v47, 49, v214
	v_add_f32_e32 v98, v98, v44
	v_cndmask_b32_e32 v45, 0, v103, vcc
	v_cmp_gt_u32_e32 vcc, s88, v46
	v_exp_f32_e32 v48, v48
	v_subrev_u32_e32 v49, 50, v214
	v_add_f32_e32 v98, v98, v45
	v_cndmask_b32_e32 v46, 0, v102, vcc
	v_cmp_gt_u32_e32 vcc, s88, v47
	v_subrev_u32_e32 v100, 51, v214
	v_add_f32_e32 v98, v46, v98
	v_cndmask_b32_e32 v47, 0, v101, vcc
	v_cmp_gt_u32_e32 vcc, s88, v49
	v_add_f32_e32 v98, v47, v98
	s_mov_b64 s[18:19], 0
	v_cndmask_b32_e32 v49, 0, v99, vcc
	v_cmp_gt_u32_e32 vcc, s88, v100
	v_add_f32_e32 v98, v49, v98
	s_nop 0
	v_cndmask_b32_e32 v100, 0, v48, vcc
	v_add_f32_e32 v98, v100, v98

.LBB0_691:
	s_waitcnt vmcnt(13)
	ds_write_b128 v208, v[42:45]
	s_waitcnt vmcnt(12)
	ds_write_b128 v208, v[46:49] offset:1152
	s_waitcnt vmcnt(11)
	ds_write_b128 v208, v[50:53] offset:2304
	s_waitcnt vmcnt(10)
	ds_write_b128 v208, v[54:57] offset:3456
	v_cvt_pk_bf16_f32 v42, v96, v104
	v_cvt_pk_bf16_f32 v43, v108, v88
	v_cvt_pk_bf16_f32 v44, v97, v86
	v_cvt_pk_bf16_f32 v45, v109, v94
	ds_read_b64_tr_b16 v[48:49], v209 offset:2304
	ds_read_b64_tr_b16 v[46:47], v209
	ds_read_b64_tr_b16 v[50:51], v209 offset:32
	ds_read_b64_tr_b16 v[66:67], v209 offset:64
	ds_read_b64_tr_b16 v[90:91], v209 offset:96
	ds_read_b64_tr_b16 v[52:53], v209 offset:2336
	ds_read_b64_tr_b16 v[68:69], v209 offset:2368
	ds_read_b64_tr_b16 v[92:93], v209 offset:2400
	s_waitcnt lgkmcnt(6)
	v_mfma_f32_16x16x32_bf16 v[54:57], v[42:45], v[46:49], v[70:73]
	s_cmp_ge_i32 s16, s18
	s_waitcnt lgkmcnt(1)
	v_mfma_f32_16x16x32_bf16 v[46:49], v[42:45], v[66:69], v[78:81]
	v_mov_b32_e32 v66, v89
	s_nop 1
	v_permlane16_swap_b32_e32 v89, v66
	v_mfma_f32_16x16x32_bf16 v[50:53], v[42:45], v[50:53], v[74:77]
	v_add_f32_e32 v66, v89, v66
	v_mov_b32_e32 v67, v66
	s_nop 1
	v_permlane32_swap_b32_e32 v66, v67
	s_waitcnt lgkmcnt(0)
	v_mfma_f32_16x16x32_bf16 v[42:45], v[42:45], v[90:93], v[82:85]
	s_cbranch_scc1 .LBB0_702
	s_lshl_b32 s12, s16, 1
	s_add_i32 s14, s17, s12
	v_and_b32_e32 v68, 3, v6
	v_lshl_add_u32 v69, v68, 1, s14
	ds_read_u16 v69, v69
	v_or_b32_e32 v68, s16, v68
	v_cmp_gt_i32_e64 s[12:13], s18, v68
	s_mov_b32 s35, 0x400001
	s_waitcnt lgkmcnt(0)
	v_lshrrev_b32_e32 v224, 8, v69
	v_and_b32_e32 v69, 0xff, v69
	v_lshlrev_b32_e32 v69, 2, v69
	v_add_u32_e32 v225, 0x12b00, v69
.Lturn_poll:
	ds_read_b32 v70, v225
	s_waitcnt lgkmcnt(0)
	v_cmp_ne_u32_e32 vcc, v70, v224
	s_and_b64 s[36:37], vcc, s[12:13]
	s_cbranch_scc0 .LBB0_702
	s_sleep 1
	s_add_i32 s35, s35, -1
	s_cmp_eq_u32 s35, 0
	s_cbranch_scc0 .Lturn_poll

.LBB0_706:
	s_or_b64 exec, exec, s[0:1]
	s_waitcnt lgkmcnt(0)
	v_add_u32_e32 v42, s16, v6
	v_cmp_gt_i32_e32 vcc, s18, v42
	s_and_b64 s[12:13], s[54:55], vcc
	s_and_saveexec_b64 s[0:1], s[12:13]
	s_cbranch_execz .LBB0_674
	v_add_u32_e32 v43, 1, v224
	ds_write_b32 v225, v43
	s_branch .LBB0_674

.LBB0_709:
	v_or_b32_e32 v14, s9, v190
	v_add_u32_e32 v15, s31, v14
	v_mov_b64_e32 v[10:11], s[6:7]
	v_mad_i64_i32 v[10:11], s[0:1], v15, s12, v[10:11]
	s_mov_b32 s9, s93
	v_lshl_add_u64 v[10:11], v[10:11], 0, s[8:9]
	v_add_co_u32_e32 v10, vcc, 0x2000, v10
	s_mov_b32 s9, 4
	s_nop 0
	v_addc_co_u32_e32 v11, vcc, 0, v11, vcc
	global_load_dwordx2 v[10:11], v[10:11], off offset:1936
	s_waitcnt vmcnt(0)
	v_lshlrev_b32_e32 v12, 16, v10
	v_and_b32_e32 v10, 0xffff0000, v10
	v_mul_f32_e32 v10, 0xbfb8aa3b, v10
	v_exp_f32_e32 v10, v10
	v_mul_f32_e32 v12, 0xbfb8aa3b, v12
	v_exp_f32_e32 v12, v12
	v_add_f32_e32 v10, 1.0, v10
	v_rcp_f32_e32 v17, v10
	v_lshlrev_b32_e32 v10, 16, v11
	v_mul_f32_e32 v10, 0xbfb8aa3b, v10
	v_exp_f32_e32 v10, v10
	v_add_f32_e32 v12, 1.0, v12
	v_rcp_f32_e32 v16, v12
	v_add_f32_e32 v10, 1.0, v10
	v_rcp_f32_e32 v18, v10
	v_and_b32_e32 v10, 0xffff0000, v11
	v_mul_f32_e32 v10, 0xbfb8aa3b, v10
	v_exp_f32_e32 v10, v10
	s_nop 0
	v_add_f32_e32 v10, 1.0, v10
	v_rcp_f32_e32 v19, v10
	v_lshl_add_u32 v10, v14, 4, 0
	v_add_u32_e32 v10, 0x10000, v10
	ds_read_b128 v[10:13], v10
	s_waitcnt lgkmcnt(0)
	v_div_scale_f32 v20, s[10:11], v10, v10, v16
	v_rcp_f32_e32 v21, v20
	v_cmp_lt_f32_e64 s[0:1], 0, v10
	v_fma_f32 v22, -v20, v21, 1.0
	v_fmac_f32_e32 v21, v22, v21
	v_div_scale_f32 v22, vcc, v16, v10, v16
	v_mul_f32_e32 v23, v22, v21
	v_fma_f32 v24, -v20, v23, v22
	v_fmac_f32_e32 v23, v24, v21
	v_fma_f32 v20, -v20, v23, v22
	v_div_fmas_f32 v20, v20, v21, v23
	v_div_fixup_f32 v10, v20, v10, v16
	v_cndmask_b32_e64 v20, 0, v10, s[0:1]
	v_div_scale_f32 v10, s[10:11], v11, v11, v17
	v_rcp_f32_e32 v16, v10
	v_cmp_lt_f32_e64 s[0:1], 0, v11
	v_lshl_add_u32 v24, v14, 10, v189
	v_fma_f32 v21, -v10, v16, 1.0
	v_fmac_f32_e32 v16, v21, v16
	v_div_scale_f32 v21, vcc, v17, v11, v17
	v_mul_f32_e32 v22, v21, v16
	v_fma_f32 v23, -v10, v22, v21
	v_fmac_f32_e32 v22, v23, v16
	v_fma_f32 v10, -v10, v22, v21
	v_div_fmas_f32 v10, v10, v16, v22
	v_div_fixup_f32 v10, v10, v11, v17
	v_cndmask_b32_e64 v21, 0, v10, s[0:1]
	v_div_scale_f32 v10, s[10:11], v12, v12, v18
	v_rcp_f32_e32 v11, v10
	v_cmp_lt_f32_e64 s[0:1], 0, v12
	v_fma_f32 v16, -v10, v11, 1.0
	v_fmac_f32_e32 v11, v16, v11
	v_div_scale_f32 v16, vcc, v18, v12, v18
	v_mul_f32_e32 v17, v16, v11
	v_fma_f32 v22, -v10, v17, v16
	v_fmac_f32_e32 v17, v22, v11
	v_fma_f32 v10, -v10, v17, v16
	v_div_fmas_f32 v10, v10, v11, v17
	v_div_fixup_f32 v10, v10, v12, v18
	v_cndmask_b32_e64 v22, 0, v10, s[0:1]
	v_div_scale_f32 v10, s[10:11], v13, v13, v19
	v_rcp_f32_e32 v11, v10
	v_cmp_lt_f32_e64 s[0:1], 0, v13
	v_fma_f32 v12, -v10, v11, 1.0
	v_fmac_f32_e32 v11, v12, v11
	v_div_scale_f32 v12, vcc, v19, v13, v19
	v_mul_f32_e32 v16, v12, v11
	v_fma_f32 v17, -v10, v16, v12
	v_fmac_f32_e32 v16, v17, v11
	v_fma_f32 v10, -v10, v16, v12
	v_div_fmas_f32 v10, v10, v11, v16
	v_div_fixup_f32 v10, v10, v13, v19
	v_cndmask_b32_e64 v23, 0, v10, s[0:1]
	v_add_u32_e32 v10, s30, v15
	v_ashrrev_i32_e32 v11, 31, v10
	v_lshlrev_b64 v[10:11], 10, v[10:11]
	v_lshl_add_u64 v[10:11], v[140:141], 0, v[10:11]
	global_load_ushort v40, v[10:11], off
	global_load_ushort v41, v[10:11], off offset:128
	global_load_ushort v42, v[10:11], off offset:256
	global_load_ushort v43, v[10:11], off offset:384
	global_load_ushort v44, v[10:11], off offset:32
	global_load_ushort v45, v[10:11], off offset:160
	global_load_ushort v46, v[10:11], off offset:288
	global_load_ushort v47, v[10:11], off offset:416
	global_load_ushort v48, v[10:11], off offset:64
	global_load_ushort v49, v[10:11], off offset:192
	global_load_ushort v50, v[10:11], off offset:320
	global_load_ushort v51, v[10:11], off offset:448
	global_load_ushort v52, v[10:11], off offset:96
	global_load_ushort v53, v[10:11], off offset:224
	global_load_ushort v54, v[10:11], off offset:352
	global_load_ushort v55, v[10:11], off offset:480
	ds_read2_b32 v[26:27], v24 offset1:16
	ds_read2_b32 v[28:29], v24 offset0:32 offset1:48
	ds_read2_b32 v[30:31], v24 offset0:64 offset1:80
	ds_read2_b32 v[32:33], v24 offset0:96 offset1:112
	ds_read2_b32 v[34:35], v24 offset0:128 offset1:144
	ds_read2_b32 v[36:37], v24 offset0:160 offset1:176
	ds_read2_b32 v[38:39], v24 offset0:192 offset1:208
	ds_read2_b32 v[56:57], v24 offset0:224 offset1:240
	s_and_b64 vcc, exec, s[4:5]
	s_mov_b64 s[4:5], 0
	s_waitcnt vmcnt(0) lgkmcnt(0)
	v_lshlrev_b32_e32 v40, 16, v40
	v_lshlrev_b32_e32 v41, 16, v41
	v_lshlrev_b32_e32 v42, 16, v42
	v_lshlrev_b32_e32 v43, 16, v43
	v_lshlrev_b32_e32 v44, 16, v44
	v_lshlrev_b32_e32 v45, 16, v45
	v_lshlrev_b32_e32 v46, 16, v46
	v_lshlrev_b32_e32 v47, 16, v47
	v_lshlrev_b32_e32 v48, 16, v48
	v_lshlrev_b32_e32 v49, 16, v49
	v_lshlrev_b32_e32 v50, 16, v50
	v_lshlrev_b32_e32 v51, 16, v51
	v_lshlrev_b32_e32 v52, 16, v52
	v_lshlrev_b32_e32 v53, 16, v53
	v_lshlrev_b32_e32 v54, 16, v54
	v_lshlrev_b32_e32 v55, 16, v55
	v_fmac_f32_e32 v40, v26, v20
	v_fmac_f32_e32 v41, v30, v21
	v_fmac_f32_e32 v42, v34, v22
	v_fmac_f32_e32 v43, v38, v23
	v_fmac_f32_e32 v44, v27, v20
	v_fmac_f32_e32 v45, v31, v21
	v_fmac_f32_e32 v46, v35, v22
	v_fmac_f32_e32 v47, v39, v23
	v_fmac_f32_e32 v48, v28, v20
	v_fmac_f32_e32 v49, v32, v21
	v_fmac_f32_e32 v50, v36, v22
	v_fmac_f32_e32 v51, v56, v23
	v_fmac_f32_e32 v52, v29, v20
	v_fmac_f32_e32 v53, v33, v21
	v_fmac_f32_e32 v54, v37, v22
	v_fmac_f32_e32 v55, v57, v23
	v_bfe_u32 v58, v40, 16, 1
	v_bfe_u32 v59, v41, 16, 1
	v_bfe_u32 v60, v42, 16, 1
	v_bfe_u32 v61, v43, 16, 1
	v_bfe_u32 v62, v44, 16, 1
	v_bfe_u32 v63, v45, 16, 1
	v_bfe_u32 v64, v46, 16, 1
	v_bfe_u32 v65, v47, 16, 1
	v_bfe_u32 v68, v48, 16, 1
	v_bfe_u32 v69, v49, 16, 1
	v_bfe_u32 v70, v50, 16, 1
	v_bfe_u32 v71, v51, 16, 1
	v_bfe_u32 v72, v52, 16, 1
	v_bfe_u32 v73, v53, 16, 1
	v_bfe_u32 v74, v54, 16, 1
	v_bfe_u32 v75, v55, 16, 1
	v_add3_u32 v40, v40, v58, s90
	v_add3_u32 v41, v41, v59, s90
	v_add3_u32 v42, v42, v60, s90
	v_add3_u32 v43, v43, v61, s90
	v_add3_u32 v44, v44, v62, s90
	v_add3_u32 v45, v45, v63, s90
	v_add3_u32 v46, v46, v64, s90
	v_add3_u32 v47, v47, v65, s90
	v_add3_u32 v48, v48, v68, s90
	v_add3_u32 v49, v49, v69, s90
	v_add3_u32 v50, v50, v70, s90
	v_add3_u32 v51, v51, v71, s90
	v_add3_u32 v52, v52, v72, s90
	v_add3_u32 v53, v53, v73, s90
	v_add3_u32 v54, v54, v74, s90
	v_add3_u32 v55, v55, v75, s90
	global_store_short_d16_hi v[10:11], v40, off
	global_store_short_d16_hi v[10:11], v41, off offset:128
	global_store_short_d16_hi v[10:11], v42, off offset:256
	global_store_short_d16_hi v[10:11], v43, off offset:384
	global_store_short_d16_hi v[10:11], v44, off offset:32
	global_store_short_d16_hi v[10:11], v45, off offset:160
	global_store_short_d16_hi v[10:11], v46, off offset:288
	global_store_short_d16_hi v[10:11], v47, off offset:416
	global_store_short_d16_hi v[10:11], v48, off offset:64
	global_store_short_d16_hi v[10:11], v49, off offset:192
	global_store_short_d16_hi v[10:11], v50, off offset:320
	global_store_short_d16_hi v[10:11], v51, off offset:448
	global_store_short_d16_hi v[10:11], v52, off offset:96
	global_store_short_d16_hi v[10:11], v53, off offset:224
	global_store_short_d16_hi v[10:11], v54, off offset:352
	global_store_short_d16_hi v[10:11], v55, off offset:480
	s_cbranch_vccnz .LBB0_709
	v_readlane_b32 s0, v254, 28
	s_add_i32 s29, s29, s0
	s_cmpk_lt_i32 s29, 0x400
	s_barrier
	s_cbranch_scc1 .LBB0_603
